# code placement: the inner K-loop heads of the GEMM phases aligned to 8 bytes (.p2align 3)
# baseline (speedup 1.0000x reference)
.LBB0_197:
	s_and_b64 s[6:7], s[30:31], exec
	s_cselect_b32 s5, s25, s35
	s_cselect_b32 s11, s24, s34
	s_cselect_b32 s21, s27, s63
	s_cselect_b32 s23, s26, s62
	s_cselect_b32 vcc_lo, s29, s37
	s_cselect_b32 vcc_hi, s28, s36
	s_add_u32 s8, s62, 0x100
	s_addc_u32 s6, s63, 0
	s_add_u32 s7, s36, 0x100
	s_addc_u32 s33, s37, 0
	s_mov_b32 s9, -2
	.p2align	3

.LBB0_281:
	v_readlane_b32 s6, v255, 3
	s_add_u32 s12, s12, s6
	s_addc_u32 s13, s13, s47
	s_add_i32 s33, s33, 1
	s_mov_b64 s[24:25], 0
	.p2align	3

.LBB0_517:
	s_and_b64 s[40:41], s[28:29], exec
	s_cselect_b32 s19, s23, s31
	s_cselect_b32 s21, s22, s30
	s_cselect_b32 s40, s25, s37
	s_cselect_b32 s41, s24, s36
	s_cselect_b32 s42, s27, s57
	s_cselect_b32 s43, s26, s56
	s_lshl_b32 s33, s34, 8
	s_lshl_b32 s34, s35, 8
	s_add_i32 s33, s33, s4
	s_or_b32 s82, s34, s5
	s_add_u32 s44, s36, 0x100
	s_addc_u32 s45, s37, 0
	s_add_u32 s46, s56, 0x100
	v_mov_b32_e32 v32, 0
	s_addc_u32 s47, s57, 0
	s_mov_b32 s48, -2
	v_mov_b32_e32 v33, v32
	v_pk_mov_b32 v[34:35], v[32:33], v[32:33]
	v_pk_mov_b32 v[36:37], v[32:33], v[32:33]
	v_pk_mov_b32 v[38:39], v[32:33], v[32:33]
	v_pk_mov_b32 v[48:49], v[32:33], v[32:33]
	v_pk_mov_b32 v[50:51], v[32:33], v[32:33]
	v_pk_mov_b32 v[52:53], v[32:33], v[32:33]
	v_pk_mov_b32 v[54:55], v[32:33], v[32:33]
	v_pk_mov_b32 v[0:1], v[32:33], v[32:33]
	v_pk_mov_b32 v[2:3], v[32:33], v[32:33]
	v_pk_mov_b32 v[4:5], v[32:33], v[32:33]
	v_pk_mov_b32 v[6:7], v[32:33], v[32:33]
	v_pk_mov_b32 v[16:17], v[32:33], v[32:33]
	v_pk_mov_b32 v[18:19], v[32:33], v[32:33]
	v_pk_mov_b32 v[20:21], v[32:33], v[32:33]
	v_pk_mov_b32 v[22:23], v[32:33], v[32:33]
	v_pk_mov_b32 v[40:41], v[32:33], v[32:33]
	v_pk_mov_b32 v[42:43], v[32:33], v[32:33]
	s_waitcnt vmcnt(4)
	v_pk_mov_b32 v[44:45], v[32:33], v[32:33]
	v_pk_mov_b32 v[46:47], v[32:33], v[32:33]
	v_pk_mov_b32 v[56:57], v[32:33], v[32:33]
	v_pk_mov_b32 v[58:59], v[32:33], v[32:33]
	v_pk_mov_b32 v[60:61], v[32:33], v[32:33]
	v_pk_mov_b32 v[62:63], v[32:33], v[32:33]
	v_pk_mov_b32 v[64:65], v[32:33], v[32:33]
	v_pk_mov_b32 v[66:67], v[32:33], v[32:33]
	v_pk_mov_b32 v[68:69], v[32:33], v[32:33]
	v_pk_mov_b32 v[70:71], v[32:33], v[32:33]
	v_pk_mov_b32 v[80:81], v[32:33], v[32:33]
	v_pk_mov_b32 v[82:83], v[32:33], v[32:33]
	v_pk_mov_b32 v[84:85], v[32:33], v[32:33]
	v_pk_mov_b32 v[86:87], v[32:33], v[32:33]
	v_pk_mov_b32 v[96:97], v[32:33], v[32:33]
	v_pk_mov_b32 v[98:99], v[32:33], v[32:33]
	v_pk_mov_b32 v[100:101], v[32:33], v[32:33]
	v_pk_mov_b32 v[102:103], v[32:33], v[32:33]
	v_pk_mov_b32 v[112:113], v[32:33], v[32:33]
	v_pk_mov_b32 v[114:115], v[32:33], v[32:33]
	v_pk_mov_b32 v[116:117], v[32:33], v[32:33]
	v_pk_mov_b32 v[118:119], v[32:33], v[32:33]
	v_pk_mov_b32 v[72:73], v[32:33], v[32:33]
	v_pk_mov_b32 v[74:75], v[32:33], v[32:33]
	v_pk_mov_b32 v[76:77], v[32:33], v[32:33]
	v_pk_mov_b32 v[78:79], v[32:33], v[32:33]
	v_pk_mov_b32 v[88:89], v[32:33], v[32:33]
	v_pk_mov_b32 v[90:91], v[32:33], v[32:33]
	v_pk_mov_b32 v[92:93], v[32:33], v[32:33]
	v_pk_mov_b32 v[94:95], v[32:33], v[32:33]
	v_pk_mov_b32 v[104:105], v[32:33], v[32:33]
	v_pk_mov_b32 v[106:107], v[32:33], v[32:33]
	v_pk_mov_b32 v[108:109], v[32:33], v[32:33]
	v_pk_mov_b32 v[110:111], v[32:33], v[32:33]
	v_pk_mov_b32 v[120:121], v[32:33], v[32:33]
	v_pk_mov_b32 v[122:123], v[32:33], v[32:33]
	v_pk_mov_b32 v[124:125], v[32:33], v[32:33]
	v_pk_mov_b32 v[126:127], v[32:33], v[32:33]
	v_pk_mov_b32 v[28:29], v[32:33], v[32:33]
	v_pk_mov_b32 v[30:31], v[32:33], v[32:33]
	v_pk_mov_b32 v[24:25], v[32:33], v[32:33]
	v_pk_mov_b32 v[26:27], v[32:33], v[32:33]
	v_pk_mov_b32 v[12:13], v[32:33], v[32:33]
	v_pk_mov_b32 v[14:15], v[32:33], v[32:33]
	v_pk_mov_b32 v[8:9], v[32:33], v[32:33]
	v_pk_mov_b32 v[10:11], v[32:33], v[32:33]
	s_branch .LBB0_519
	.p2align	3

.LBB0_694:
	s_xor_b64 s[34:35], s[56:57], -1
	s_and_b64 s[62:63], s[56:57], exec
	s_cselect_b32 s23, s27, s7
	s_cselect_b32 s25, s26, s6
	s_cselect_b32 s86, s29, s15
	s_cselect_b32 s87, s28, s14
	s_cselect_b32 s96, s31, s17
	s_cselect_b32 s97, s30, s16
	s_mov_b32 vcc_lo, -2
	.p2align	3

.LBB0_1035:
	v_mbcnt_lo_u32_b32 v4, -1, 0
	v_mbcnt_hi_u32_b32 v4, -1, v4
	s_add_u32 s19, s50, 0x100
	v_add_u32_e32 v4, s0, v4
	v_lshl_add_u32 v4, v4, 4, 0
	v_add_u32_e32 v4, 0x21000, v4
	s_addc_u32 s25, s51, 0
	ds_write_b128 v4, v[0:3]
	s_add_u32 s81, s56, 0x100
	s_addc_u32 s82, s57, 0
	s_mov_b32 s83, -2
	s_branch .LBB0_1037
	.p2align	3

.LBB0_1152:
	s_and_b64 s[50:51], s[26:27], exec
	s_cselect_b32 s5, s21, s35
	s_cselect_b32 s29, s20, s34
	s_cselect_b32 s72, s23, s37
	s_cselect_b32 s73, s22, s36
	s_cselect_b32 s74, s25, s47
	s_cselect_b32 s75, s24, s46
	s_add_u32 s76, s36, 0x100
	s_addc_u32 s77, s37, 0
	s_add_u32 s78, s46, 0x100
	s_addc_u32 s79, s47, 0
	s_mov_b32 s80, -2
	s_waitcnt vmcnt(4)
	.p2align	3

.LBB0_1181:
	s_add_i32 s65, s65, s42
	s_add_i32 s67, s67, s64
	s_add_i32 s68, s68, s66
	s_mov_b64 s[18:19], 0
	.p2align	3

.LBB0_1340:
	s_xor_b64 s[26:27], s[30:31], -1
	s_and_b64 s[34:35], s[30:31], exec
	s_cselect_b32 s17, s21, s1
	s_cselect_b32 s19, s20, s0
	s_cselect_b32 s65, s23, s9
	s_cselect_b32 s66, s22, s8
	s_cselect_b32 s67, s25, s11
	s_cselect_b32 s68, s24, s10
	s_mov_b32 s69, -2
	.p2align	3
